# v17 + prologue conversion jobs dealt over all waves by a running tile offset (small jobs no longer pile onto the low-numbered workgroups)
# speedup vs baseline: 1.0100x; 1.0085x over previous
; #define LAS __attribute__((address_space(3)))
; DI void tr_tile(const float* src, int N, int k0, int n0, float scale, bf16_t* dst_row0  , int K, bf16_t* dst_lo, LAS bf16_t* T, int lane) {
; #pragma unroll 4
;     for (int it = 0; it < 8; ++it) {
;         const int kk = it * 8 + 2 * (lane >> 4), c4 = (lane & 15) * 4;
;         const f32x4 v0 = *(const f32x4*)(src + (size_t)(k0 + kk) * N + n0 + c4) * scale, v1 = *(const f32x4*)(src + (size_t)(k0 + kk + 1) * N + n0 + c4) * scale;
; #pragma unroll
;         for (int j = 0; j < 4; ++j) *(LAS unsigned*)(T + (c4 + j) * 72 + kk) = pk_bf16(v0[j], v1[j]);
;     }
;     __builtin_amdgcn_s_waitcnt(0xc07f);
; #pragma unroll 4
;     for (int it = 0; it < 8; ++it) {
;         const int n = it * 8 + (lane >> 3), kc = (lane & 7) * 8;
;         const u32x4 w = *(const LAS u32x4*)(T + n * 72 + kc);
;         *(u32x4*)(dst_row0 + (size_t)n * K + kc) = w;
; DI void phase_prologue(const Ctx& c) {
;     const Params p = load_params(c.kp); char* ws = p.ws;
;     LAS bf16_t* T = (LAS bf16_t*)(c.lds) + c.wid * (64 * 72);
;     const int gw = c.blk * 8 + c.wid, nw = c.G * 8;
; #pragma unroll 1
;     for (int j = 0; j < 10; ++j) {
;         Job jb;
;         switch (j) {
;             case 0: jb = Job{p.rg_w_in, (bf16_t*)(ws + WS_WIN), 2, 1024, 2048, 0}; break;
;             case 1: jb = Job{p.rg_w_gates, (bf16_t*)(ws + WS_WG), 8, 256, 512, 1}; break;
;             case 2: jb = Job{p.rg_w_out, (bf16_t*)(ws + WS_WOUT), 2, 1024, 1024, 0}; break;
;             case 3: jb = Job{p.attn_w_qkv, (bf16_t*)(ws + WS_WQKV), 2, 1024, 1536, 2}; break;
;             case 4: jb = Job{p.attn_w_o, (bf16_t*)(ws + WS_WO), 2, 1024, 1024, 0}; break;
;             case 5: jb = Job{p.ex_w_gu, (bf16_t*)(ws + WS_WEGU), 256, 1024, 512, 1}; break;
;             case 6: jb = Job{p.ex_w_down, (bf16_t*)(ws + WS_WED), 256, 256, 1024, 0}; break;
;             case 7: jb = Job{p.sh_w_gu, (bf16_t*)(ws + WS_WSGU), 4, 1024, 512, 1}; break;
;             case 8: jb = Job{p.sh_w_down, (bf16_t*)(ws + WS_WSD), 4, 256, 1024, 0}; break;
;             default: jb = Job{p.router_w, (bf16_t*)(ws + WS_WRH), 4, 1024, 64, 3}; break;
;         }
;         const int tk = jb.K / 64, tn = jb.N / 64, per = tk * tn, total = jb.count * per;
;         for (int t = gw; t < total; t += nw) {
.LBB0_4:
	v_writelane_b32 v255, s6, 2
	s_or_b64 exec, exec, s[0:1]
	s_lshr_b32 s1, s2, 6
	v_mov_b32_e32 v0, 0
	v_writelane_b32 v255, s1, 3
	s_mov_b64 s[36:37], s[92:93]
	v_mbcnt_lo_u32_b32 v0, -1, v0
	v_mbcnt_hi_u32_b32 v0, -1, v0
	v_lshl_add_u32 v4, s1, 6, v0
	s_mov_b32 s0, s96
	s_mov_b32 s2, s97
	s_lshl_b32 s3, s0, 3
	s_mul_i32 s22, s1, 0x2400
	s_add_i32 s1, s3, s1
	s_lshl_b32 s3, s2, 3
	s_load_dwordx2 s[20:21], s[36:37], 0xb8
	s_load_dwordx4 s[16:19], s[36:37], 0x0
	s_load_dwordx2 s[24:25], s[36:37], 0x10
	s_load_dwordx2 s[26:27], s[36:37], 0x30
	s_load_dwordx4 s[12:15], s[36:37], 0x40
	s_load_dwordx2 s[28:29], s[36:37], 0x50
	s_load_dwordx2 s[30:31], s[36:37], 0x60
	s_load_dwordx2 s[34:35], s[36:37], 0x80
	s_load_dwordx8 s[4:11], s[36:37], 0x90
	s_waitcnt lgkmcnt(0)
	s_add_u32 s36, s20, 0x19d40800
	s_addc_u32 s37, s21, 0
	s_add_u32 s38, s20, 0x19940800
	s_addc_u32 s39, s21, 0
	s_add_u32 s40, s20, 0x11940800
	s_addc_u32 s41, s21, 0
	s_add_u32 s42, s20, 0x1940800
	s_addc_u32 s43, s21, 0
	s_add_u32 s44, s20, 0x1540800
	s_addc_u32 s45, s21, 0
	s_add_u32 s46, s20, 0xf40800
	s_addc_u32 s47, s21, 0
	v_lshrrev_b32_e32 v0, 3, v4
	s_add_u32 s48, s20, 0xb40800
	v_and_b32_e32 v5, 6, v0
	v_lshlrev_b32_e32 v0, 2, v4
	s_addc_u32 s49, s21, 0
	v_and_b32_e32 v14, 60, v0
	s_movk_i32 s33, 0x90
	v_mov_b32_e32 v0, s22
	s_add_u32 s50, s20, 0x940800
	v_mad_u32_u24 v0, v14, s33, v0
	v_lshrrev_b32_e32 v2, 2, v4
	s_addc_u32 s51, s21, 0
	v_and_or_b32 v0, v2, 12, v0
	s_add_u32 s52, s20, 0x140800
	v_bfe_u32 v8, v4, 3, 3
	v_add_u32_e32 v38, 0, v0
	v_lshlrev_b32_e32 v0, 4, v4
	v_mov_b32_e32 v1, 0
	s_addc_u32 s53, s21, 0
	v_and_b32_e32 v0, 0x70, v0
	v_lshlrev_b32_e32 v2, 1, v8
	v_mul_u32_u24_e32 v8, 0x90, v8
	s_add_u32 s54, s20, 0x19f40800
	v_or_b32_e32 v8, s22, v8
	v_lshl_add_u64 v[12:13], s[20:21], 0, v[0:1]
	s_mov_b64 s[56:57], 0x19fc0800
	s_mov_b32 s23, 0
	s_addc_u32 s55, s21, 0
	v_mov_b32_e32 v3, v1
	v_or_b32_e32 v6, 48, v2
	v_mov_b32_e32 v7, v1
	v_add3_u32 v39, v8, v0, 0
	v_or_b32_e32 v8, 32, v2
	v_mov_b32_e32 v9, v1
	v_or_b32_e32 v10, 16, v2
	v_mov_b32_e32 v11, v1
	v_lshl_add_u64 v[12:13], v[12:13], 0, s[56:57]
	v_mov_b32_e32 v40, 0x3e000000
	v_lshlrev_b32_e32 v14, 2, v14
	v_mov_b32_e32 v15, v1
	s_mov_b32 s33, 0
	s_mov_b32 s95, 0
	s_branch .LBB0_6

; DI void phase_prologue(const Ctx& c) {
;     ...
;         const int tk = jb.K / 64, tn = jb.N / 64, per = tk * tn, total = jb.count * per;
;         for (int t = gw; t < total; t += nw) {
;             const int mi = t / per, r = t % per, kt = r / tn, ntl = r % tn;
.LBB0_39:
	s_lshr_b32 s65, s22, 6
	s_lshr_b32 s73, s72, 6
	s_mul_i32 s74, s73, s65
	s_mul_i32 s75, s74, s64
	s_sub_i32 s94, s1, s95
	s_and_b32 s94, s94, 0x7ff
	s_add_i32 s95, s95, s75
	s_cmp_ge_i32 s94, s75
	s_cbranch_scc1 .LBB0_5
	v_cvt_f32_u32_e32 v16, s74
	v_cvt_f32_u32_e32 v17, s73
	s_sub_i32 s68, 0, s74
	s_sub_i32 s69, 0, s73
	v_rcp_iflag_f32_e32 v16, v16
	v_rcp_iflag_f32_e32 v17, v17
	s_mul_i32 s64, s72, s22
	s_mov_b32 s65, s23
	v_mul_f32_e32 v16, 0x4f7ffffe, v16
	v_mul_f32_e32 v17, 0x4f7ffffe, v17
	v_cvt_u32_f32_e32 v16, v16
	v_cvt_u32_f32_e32 v17, v17
	v_readfirstlane_b32 s70, v16
	v_readfirstlane_b32 s71, v17
	s_mul_i32 s68, s68, s70
	s_mul_hi_u32 s68, s70, s68
	s_mul_i32 s69, s69, s71
	s_add_i32 s76, s70, s68
	s_mul_hi_u32 s68, s71, s69
	s_add_i32 s77, s71, s68
	v_lshl_add_u64 v[16:17], s[66:67], 0, v[0:1]
	s_lshl_b64 s[66:67], s[64:65], 1
	s_lshl_b64 s[68:69], s[22:23], 6
	s_mov_b32 s65, s94
	s_branch .LBB0_42
